# rwkv_chunk S4: 8 wave-wide sums via row_bcast DPP (same operand order) instead of 4 readlanes + 2 movs + pk_add + add
# baseline (speedup 1.0000x reference)
; __device__ __forceinline__ float bf2f(unsigned v) { return __uint_as_float(v << 16); }
; #define DPPF(v, ctrl) __int_as_float(__builtin_amdgcn_update_dpp(0, __float_as_int(v), (ctrl), 0xf, 0xf, false))
; __device__ __forceinline__ void lds_st_bf16(LAS unsigned char* base, int idx, float v) { *(LAS bf16_t*)(base + idx * 2) = (bf16_t)f2bf(v); }
; __device__ __forceinline__ float row16_sum(float v) {
;     v += DPPF(v, 0xB1); v += DPPF(v, 0x4E); v += DPPF(v, 0x141); v += DPPF(v, 0x140); return v;
; }
; __device__ __forceinline__ float wave_sum(float v) {
;     v = row16_sum(v);
;     const int iv = __float_as_int(v);
;     return (__int_as_float(__builtin_amdgcn_readlane(iv, 0)) + __int_as_float(__builtin_amdgcn_readlane(iv, 16))) + (__int_as_float(__builtin_amdgcn_readlane(iv, 32)) + __int_as_float(__builtin_amdgcn_readlane(iv, 48)));
; }
; __device__ __forceinline__ void phase_rwkv_chunk(const Ctx& c, const Args& a, int layer, const bf16_t* proj, const bf16_t* wlb, const bf16_t* alb, bf16_t* rwu, float* bonusg) {
;     ...
;             for (int i = 0; i < 8; ++i) { const int tt = wave * 8 + i, t = t0 + tt;
;                 const float Lc = lcs[i] + off, al = als[i];
;                 const float rc = bf2f(rraw[i + 1]), kc = bf2f(kraw[i + 1]), vc = bf2f(vraw[i + 1]);
;                 const float r = rc + (bf2f(rraw[i]) - rc) * mur, k = kc + (bf2f(kraw[i]) - kc) * muk, v = vc + (bf2f(vraw[i]) - vc) * muv;
;                 float kk = k * kkw; const float n2 = wave_sum(kk * kk); kk = kk * rsqrtf(fmaxf(n2, 1e-24f));
;                 const float kp = k * (1.0f + (al - 1.0f) * kaw), av = -kk, bv = kk * al;
;                 const float eW = __expf(Lc), eInv = __builtin_amdgcn_rcpf(eW), eC = eTot * eInv; const float eWex = eWprev; eWprev = eW;
;                 lds_st_bf16(L + RC_AT, tt * 72 + j, av * eWex); tA[i] = av * eWex;
;                 lds_st_bf16(L + RC_RT, tt * 72 + j, r * eW); lds_st_bf16(L + RC_BT, tt * 72 + j, bv * eInv); lds_st_bf16(L + RC_KT, tt * 72 + j, kp * eInv);
;                 tV[i] = v; tB[i] = bv * eC; tK[i] = kp * eC;
;                 const float bon = wave_sum(r * kp * rk); if (lane == 0) bonusg[(size_t)t * 8 + h] = bon; }
.LBB0_699:
	v_readlane_b32 s14, v254, 45
	v_readlane_b32 s15, v254, 46
	s_lshl_b32 s29, s52, 3
	v_lshlrev_b32_e32 v10, 16, v37
	v_cndmask_b32_e64 v4, 0, v4, s[14:15]
	v_readlane_b32 s14, v254, 47
	v_readlane_b32 s15, v254, 48
	s_andn2_b32 s29, s29, 63
	v_add_f32_e32 v10, v171, v10
	v_cndmask_b32_e64 v11, 0, v11, s[14:15]
	v_readlane_b32 s14, v254, 49
	v_readlane_b32 s15, v254, 50
	v_add_f32_e32 v4, v4, v11
	v_mul_f32_e32 v10, 0xbfb8aa3b, v10
	v_cndmask_b32_e64 v8, 0, v8, s[14:15]
	v_readlane_b32 s14, v254, 51
	v_readlane_b32 s15, v254, 52
	v_add_f32_e32 v4, v4, v8
	v_cndmask_b32_e64 v8, 0, v9, s[38:39]
	v_cndmask_b32_e64 v6, 0, v6, s[14:15]
	v_readlane_b32 s14, v254, 53
	v_add_f32_e32 v4, v4, v8
	v_readlane_b32 s15, v254, 54
	v_add_f32_e32 v4, v4, v6
	v_exp_f32_e32 v10, v10
	v_cndmask_b32_e64 v6, 0, v7, s[14:15]
	v_readlane_b32 s14, v254, 55
	v_readlane_b32 s15, v254, 56
	v_add_f32_e32 v4, v4, v6
	v_lshlrev_b32_e32 v7, 16, v47
	v_cndmask_b32_e64 v2, 0, v2, s[14:15]
	v_readlane_b32 s14, v254, 57
	v_readlane_b32 s15, v254, 58
	v_add_f32_e32 v2, v4, v2
	v_sub_f32_e32 v0, 0, v0
	v_cndmask_b32_e64 v3, 0, v3, s[14:15]
	v_add_f32_e32 v22, v2, v3
	v_mul_f32_e32 v2, 0x3fb8aa3b, v22
	v_exp_f32_e32 v8, v2
	v_lshlrev_b32_e32 v2, 16, v50
	v_sub_f32_e32 v2, v2, v7
	v_fma_f32 v4, v2, v176, v7
	v_mul_f32_e32 v11, v4, v172
	v_mul_f32_e32 v2, v11, v11
	v_mov_b32_e32 v3, v1
	s_lshl_b32 s14, s20, 2
	v_readlane_b32 s15, v252, 23
	v_mov_b32_dpp v3, v2 quad_perm:[1,0,3,2] row_mask:0xf bank_mask:0xf
	v_fmac_f32_e32 v3, v11, v11
	s_add_u32 s22, s15, s14
	v_readlane_b32 s14, v252, 24
	v_add_f32_dpp v2, v3, v3 quad_perm:[2,3,0,1] row_mask:0xf bank_mask:0xf bound_ctrl:1
	s_addc_u32 s28, s14, 0
	v_add_f32_e32 v0, v0, v22
	v_add_f32_dpp v2, v2, v2 row_half_mirror row_mask:0xf bank_mask:0xf bound_ctrl:1
	v_mul_f32_e32 v0, 0x3fb8aa3b, v0
	v_exp_f32_e32 v9, v0
	v_add_f32_dpp v2, v2, v2 row_mirror row_mask:0xf bank_mask:0xf bound_ctrl:1
	v_add_f32_e32 v10, 1.0, v10
	s_nop 1
	v_add_f32_dpp v2, v2, v2 row_bcast:15 row_mask:0xa bank_mask:0xf
	s_nop 1
	v_add_f32_dpp v2, v2, v2 row_bcast:31 row_mask:0xc bank_mask:0xf
	s_nop 1
	v_readlane_b32 s20, v2, 63
	s_nop 1
	v_rcp_f32_e32 v18, v10
	v_mov_b32_e32 v2, s20
	v_max_f32_e32 v2, 0x179abe15, v2
	v_rsq_f32_e32 v2, v2
	v_lshlrev_b32_e32 v6, 16, v53
	v_lshlrev_b32_e32 v10, 16, v46
	v_sub_f32_e32 v0, v10, v6
	v_fma_f32 v20, v0, v175, v6
	v_mul_f32_e32 v0, v11, v2
	v_rcp_f32_e32 v11, v9
	v_add_f32_e32 v2, -1.0, v18
	v_fma_f32 v10, v173, v2, 1.0
	v_mul_f32_e32 v18, v18, v0
	v_mul_f32_e64 v0, v8, -v0
	v_pk_mul_f32 v[2:3], v[4:5], v[10:11]
	v_cvt_pk_bf16_f32 v4, v0, s0
	ds_write_b16 v127, v4 offset:52992
	v_mul_f32_e32 v4, v20, v9
	v_cvt_pk_bf16_f32 v4, v4, s0
	v_add_u32_e32 v8, 0x11700, v127
	ds_write_b16 v8, v4
	v_mul_f32_e32 v4, v11, v18
	v_cvt_pk_bf16_f32 v4, v4, s0
	v_add_u32_e32 v8, 0x13b00, v127
	ds_write_b16 v8, v4
	v_mul_f32_e32 v4, v2, v11
	v_cvt_pk_bf16_f32 v4, v4, s0
	v_add_u32_e32 v8, 0x15f00, v127
	ds_write_b16 v8, v4
	v_mul_f32_e32 v4, v20, v2
	v_mul_f32_e32 v8, v174, v4
	v_mov_b32_e32 v10, v1
	s_nop 1
	v_mov_b32_dpp v10, v8 quad_perm:[1,0,3,2] row_mask:0xf bank_mask:0xf
	v_fmac_f32_e32 v10, v174, v4
	s_nop 1
	v_add_f32_dpp v4, v10, v10 quad_perm:[2,3,0,1] row_mask:0xf bank_mask:0xf bound_ctrl:1
	s_nop 1
	v_add_f32_dpp v4, v4, v4 row_half_mirror row_mask:0xf bank_mask:0xf bound_ctrl:1
	s_nop 1
	v_add_f32_dpp v4, v4, v4 row_mirror row_mask:0xf bank_mask:0xf bound_ctrl:1
	s_nop 0
	v_readlane_b32 s20, v4, 0
	v_readlane_b32 s42, v4, 16
	v_readlane_b32 s21, v4, 32
	v_readlane_b32 s53, v4, 48
	s_and_saveexec_b64 s[14:15], s[36:37]
	s_cbranch_execz .LBB0_701
	s_add_i32 s56, s29, s62
	s_ashr_i32 s57, s56, 31
	s_lshl_b64 s[56:57], s[56:57], 5
	v_mov_b32_e32 v10, s42
	v_mov_b32_e32 v11, s53
	s_add_u32 s56, s22, s56
	v_pk_add_f32 v[10:11], s[20:21], v[10:11]
	s_addc_u32 s57, s28, s57
	v_add_f32_e32 v4, v10, v11
	global_store_dword v1, v4, s[56:57]
.LBB0_701:
	s_or_b64 exec, exec, s[14:15]
	v_lshlrev_b32_e32 v4, 16, v39
	v_add_f32_e32 v4, v171, v4
	v_mul_f32_e32 v4, 0xbfb8aa3b, v4
	v_exp_f32_e32 v4, v4
	v_add_f32_e32 v20, v17, v22
	v_lshlrev_b32_e32 v17, 16, v59
	v_mov_b32_e32 v11, v1
	v_add_f32_e32 v4, 1.0, v4
	v_rcp_f32_e32 v21, v4
	v_sub_f32_e32 v4, v7, v17
	v_fma_f32 v4, v4, v176, v17
	v_mul_f32_e32 v7, v4, v172
	v_mul_f32_e32 v10, v7, v7
	v_lshlrev_b32_e32 v8, 16, v58
	v_sub_f32_e32 v6, v6, v8
	v_mov_b32_dpp v11, v10 quad_perm:[1,0,3,2] row_mask:0xf bank_mask:0xf
	v_fmac_f32_e32 v11, v7, v7
	v_fma_f32 v23, v6, v175, v8
	v_add_f32_e32 v6, -1.0, v21
	v_add_f32_dpp v10, v11, v11 quad_perm:[2,3,0,1] row_mask:0xf bank_mask:0xf bound_ctrl:1
	v_fma_f32 v24, v173, v6, 1.0
	s_nop 0
	v_add_f32_dpp v10, v10, v10 row_half_mirror row_mask:0xf bank_mask:0xf bound_ctrl:1
	s_nop 1
	v_add_f32_dpp v10, v10, v10 row_mirror row_mask:0xf bank_mask:0xf bound_ctrl:1
	s_nop 0
	s_nop 1
	v_add_f32_dpp v10, v10, v10 row_bcast:15 row_mask:0xa bank_mask:0xf
	s_nop 1
	v_add_f32_dpp v10, v10, v10 row_bcast:31 row_mask:0xc bank_mask:0xf
	s_nop 1
	v_readlane_b32 s20, v10, 63
	s_nop 1
	s_nop 0
	v_mov_b32_e32 v10, s20
	v_mul_f32_e32 v11, 0x3fb8aa3b, v20
	v_exp_f32_e32 v11, v11
	v_max_f32_e32 v10, 0x179abe15, v10
	v_rsq_f32_e32 v10, v10
	v_rcp_f32_e32 v25, v11
	v_mul_f32_e32 v10, v7, v10
	v_mul_f32_e64 v20, v9, -v10
	v_pk_mul_f32 v[6:7], v[4:5], v[24:25]
	v_cvt_pk_bf16_f32 v4, v20, s0
	ds_write_b16 v128, v4 offset:52992
	v_mul_f32_e32 v4, v23, v11
	v_mul_f32_e32 v21, v21, v10
	v_cvt_pk_bf16_f32 v4, v4, s0
	v_add_u32_e32 v9, 0x11700, v128
	ds_write_b16 v9, v4
	v_mul_f32_e32 v4, v25, v21
	v_cvt_pk_bf16_f32 v4, v4, s0
	v_add_u32_e32 v9, 0x13b00, v128
	ds_write_b16 v9, v4
	v_mul_f32_e32 v4, v6, v25
	v_cvt_pk_bf16_f32 v4, v4, s0
	v_add_u32_e32 v9, 0x15f00, v128
	ds_write_b16 v9, v4
	v_mul_f32_e32 v4, v23, v6
	v_mul_f32_e32 v9, v174, v4
	v_mov_b32_e32 v10, v1
	s_nop 1
	v_mov_b32_dpp v10, v9 quad_perm:[1,0,3,2] row_mask:0xf bank_mask:0xf
	v_fmac_f32_e32 v10, v174, v4
	s_nop 1
	v_add_f32_dpp v4, v10, v10 quad_perm:[2,3,0,1] row_mask:0xf bank_mask:0xf bound_ctrl:1
	s_nop 1
	v_add_f32_dpp v4, v4, v4 row_half_mirror row_mask:0xf bank_mask:0xf bound_ctrl:1
	s_nop 1
	v_add_f32_dpp v4, v4, v4 row_mirror row_mask:0xf bank_mask:0xf bound_ctrl:1
	s_nop 0
	v_readlane_b32 s20, v4, 0
	v_readlane_b32 s42, v4, 16
	v_readlane_b32 s21, v4, 32
	v_readlane_b32 s53, v4, 48
	s_and_saveexec_b64 s[14:15], s[36:37]
	s_cbranch_execz .LBB0_703
	v_readlane_b32 s56, v254, 59
	s_add_i32 s56, s29, s56
	s_ashr_i32 s57, s56, 31
	s_lshl_b64 s[56:57], s[56:57], 5
	v_mov_b32_e32 v24, s42
	v_mov_b32_e32 v25, s53
	s_add_u32 s56, s22, s56
	v_pk_add_f32 v[24:25], s[20:21], v[24:25]
	s_addc_u32 s57, s28, s57
	v_add_f32_e32 v4, v24, v25
	global_store_dword v1, v4, s[56:57]
; __device__ __forceinline__ float bf2f(unsigned v) { return __uint_as_float(v << 16); }
; #define DPPF(v, ctrl) __int_as_float(__builtin_amdgcn_update_dpp(0, __float_as_int(v), (ctrl), 0xf, 0xf, false))
; __device__ __forceinline__ void lds_st_bf16(LAS unsigned char* base, int idx, float v) { *(LAS bf16_t*)(base + idx * 2) = (bf16_t)f2bf(v); }
; __device__ __forceinline__ float row16_sum(float v) {
;     v += DPPF(v, 0xB1); v += DPPF(v, 0x4E); v += DPPF(v, 0x141); v += DPPF(v, 0x140); return v;
; }
; __device__ __forceinline__ float wave_sum(float v) {
;     v = row16_sum(v);
;     const int iv = __float_as_int(v);
;     return (__int_as_float(__builtin_amdgcn_readlane(iv, 0)) + __int_as_float(__builtin_amdgcn_readlane(iv, 16))) + (__int_as_float(__builtin_amdgcn_readlane(iv, 32)) + __int_as_float(__builtin_amdgcn_readlane(iv, 48)));
; }
; __device__ __forceinline__ void phase_rwkv_chunk(const Ctx& c, const Args& a, int layer, const bf16_t* proj, const bf16_t* wlb, const bf16_t* alb, bf16_t* rwu, float* bonusg) {
;     ...
;             for (int i = 0; i < 8; ++i) { const int tt = wave * 8 + i, t = t0 + tt;
;                 const float Lc = lcs[i] + off, al = als[i];
;                 const float rc = bf2f(rraw[i + 1]), kc = bf2f(kraw[i + 1]), vc = bf2f(vraw[i + 1]);
;                 const float r = rc + (bf2f(rraw[i]) - rc) * mur, k = kc + (bf2f(kraw[i]) - kc) * muk, v = vc + (bf2f(vraw[i]) - vc) * muv;
;                 float kk = k * kkw; const float n2 = wave_sum(kk * kk); kk = kk * rsqrtf(fmaxf(n2, 1e-24f));
;                 const float kp = k * (1.0f + (al - 1.0f) * kaw), av = -kk, bv = kk * al;
;                 const float eW = __expf(Lc), eInv = __builtin_amdgcn_rcpf(eW), eC = eTot * eInv; const float eWex = eWprev; eWprev = eW;
;                 lds_st_bf16(L + RC_AT, tt * 72 + j, av * eWex); tA[i] = av * eWex;
;                 lds_st_bf16(L + RC_RT, tt * 72 + j, r * eW); lds_st_bf16(L + RC_BT, tt * 72 + j, bv * eInv); lds_st_bf16(L + RC_KT, tt * 72 + j, kp * eInv);
;                 tV[i] = v; tB[i] = bv * eC; tK[i] = kp * eC;
;                 const float bon = wave_sum(r * kp * rk); if (lane == 0) bonusg[(size_t)t * 8 + h] = bon; }
.LBB0_703:
	s_or_b64 exec, exec, s[14:15]
	v_lshlrev_b32_e32 v4, 16, v41
	v_add_f32_e32 v4, v171, v4
	v_mul_f32_e32 v4, 0xbfb8aa3b, v4
	v_exp_f32_e32 v4, v4
	v_lshlrev_b32_e32 v25, 16, v57
	v_add_f32_e32 v9, v15, v22
	v_mov_b32_e32 v24, v1
	v_add_f32_e32 v4, 1.0, v4
	v_rcp_f32_e32 v23, v4
	v_sub_f32_e32 v4, v17, v25
	v_fma_f32 v4, v4, v176, v25
	v_mul_f32_e32 v17, v4, v172
	v_mul_f32_e32 v15, v17, v17
	v_mul_f32_e32 v9, 0x3fb8aa3b, v9
	v_lshlrev_b32_e32 v10, 16, v62
	v_mov_b32_dpp v24, v15 quad_perm:[1,0,3,2] row_mask:0xf bank_mask:0xf
	v_fmac_f32_e32 v24, v17, v17
	v_sub_f32_e32 v8, v8, v10
	v_fma_f32 v28, v8, v175, v10
	v_add_f32_dpp v15, v24, v24 quad_perm:[2,3,0,1] row_mask:0xf bank_mask:0xf bound_ctrl:1
	v_add_f32_e32 v8, -1.0, v23
	s_nop 0
	v_add_f32_dpp v15, v15, v15 row_half_mirror row_mask:0xf bank_mask:0xf bound_ctrl:1
	s_nop 1
	v_add_f32_dpp v15, v15, v15 row_mirror row_mask:0xf bank_mask:0xf bound_ctrl:1
	s_nop 0
	v_mov_b32_e32 v26, v15
	s_nop 1
	v_add_f32_dpp v26, v26, v26 row_bcast:15 row_mask:0xa bank_mask:0xf
	s_nop 1
	v_add_f32_dpp v26, v26, v26 row_bcast:31 row_mask:0xc bank_mask:0xf
	s_nop 1
	v_readlane_b32 s20, v26, 63
	s_nop 1
	s_nop 0
	v_mov_b32_e32 v15, s20
	v_max_f32_e32 v15, 0x179abe15, v15
	v_rsq_f32_e32 v24, v15
	v_exp_f32_e32 v15, v9
	v_fma_f32 v26, v173, v8, 1.0
	v_mul_f32_e32 v17, v17, v24
	v_rcp_f32_e32 v27, v15
	v_mul_f32_e32 v24, v23, v17
	v_mul_f32_e64 v23, v11, -v17
	v_add_u32_e32 v11, 0x11700, v129
	v_pk_mul_f32 v[8:9], v[4:5], v[26:27]
	v_cvt_pk_bf16_f32 v4, v23, s0
	ds_write_b16 v129, v4 offset:52992
	v_mul_f32_e32 v4, v28, v15
	v_cvt_pk_bf16_f32 v4, v4, s0
	ds_write_b16 v11, v4
	v_mul_f32_e32 v4, v27, v24
	v_cvt_pk_bf16_f32 v4, v4, s0
	v_add_u32_e32 v11, 0x13b00, v129
	ds_write_b16 v11, v4
	v_mul_f32_e32 v4, v8, v27
	v_cvt_pk_bf16_f32 v4, v4, s0
	v_add_u32_e32 v11, 0x15f00, v129
	ds_write_b16 v11, v4
	v_mul_f32_e32 v4, v28, v8
	v_mul_f32_e32 v11, v174, v4
	v_mov_b32_e32 v17, v1
	s_nop 1
	v_mov_b32_dpp v17, v11 quad_perm:[1,0,3,2] row_mask:0xf bank_mask:0xf
	v_fmac_f32_e32 v17, v174, v4
	s_nop 1
	v_add_f32_dpp v4, v17, v17 quad_perm:[2,3,0,1] row_mask:0xf bank_mask:0xf bound_ctrl:1
	s_nop 1
	v_add_f32_dpp v4, v4, v4 row_half_mirror row_mask:0xf bank_mask:0xf bound_ctrl:1
	s_nop 1
	v_add_f32_dpp v4, v4, v4 row_mirror row_mask:0xf bank_mask:0xf bound_ctrl:1
	s_nop 0
	v_readlane_b32 s20, v4, 0
	v_readlane_b32 s42, v4, 16
	v_readlane_b32 s21, v4, 32
	v_readlane_b32 s53, v4, 48
	s_and_saveexec_b64 s[14:15], s[36:37]
	s_cbranch_execz .LBB0_705
	v_readlane_b32 s56, v254, 60
	s_add_i32 s56, s29, s56
	s_ashr_i32 s57, s56, 31
	s_lshl_b64 s[56:57], s[56:57], 5
	v_mov_b32_e32 v26, s42
	v_mov_b32_e32 v27, s53
	s_add_u32 s56, s22, s56
	v_pk_add_f32 v[26:27], s[20:21], v[26:27]
	s_addc_u32 s57, s28, s57
	v_add_f32_e32 v4, v26, v27
	global_store_dword v1, v4, s[56:57]
.LBB0_705:
	s_or_b64 exec, exec, s[14:15]
	v_lshlrev_b32_e32 v4, 16, v43
	v_add_f32_e32 v4, v171, v4
	v_mul_f32_e32 v4, 0xbfb8aa3b, v4
	v_exp_f32_e32 v4, v4
	v_lshlrev_b32_e32 v27, 16, v66
	v_mov_b32_e32 v28, v1
	v_add_f32_e32 v11, v12, v22
	v_add_f32_e32 v4, 1.0, v4
	v_rcp_f32_e32 v26, v4
	v_sub_f32_e32 v4, v25, v27
	v_fma_f32 v4, v4, v176, v27
	v_mul_f32_e32 v25, v4, v172
	v_mul_f32_e32 v17, v25, v25
	v_mul_f32_e32 v11, 0x3fb8aa3b, v11
	v_lshlrev_b32_e32 v12, 16, v64
	v_mov_b32_dpp v28, v17 quad_perm:[1,0,3,2] row_mask:0xf bank_mask:0xf
	v_fmac_f32_e32 v28, v25, v25
	v_sub_f32_e32 v10, v10, v12
	v_fma_f32 v34, v10, v175, v12
	v_add_f32_dpp v17, v28, v28 quad_perm:[2,3,0,1] row_mask:0xf bank_mask:0xf bound_ctrl:1
	v_add_f32_e32 v10, -1.0, v26
	s_nop 0
	v_add_f32_dpp v17, v17, v17 row_half_mirror row_mask:0xf bank_mask:0xf bound_ctrl:1
	s_nop 1
	v_add_f32_dpp v17, v17, v17 row_mirror row_mask:0xf bank_mask:0xf bound_ctrl:1
	s_nop 0
	v_mov_b32_e32 v28, v17
	s_nop 1
	v_add_f32_dpp v28, v28, v28 row_bcast:15 row_mask:0xa bank_mask:0xf
	s_nop 1
	v_add_f32_dpp v28, v28, v28 row_bcast:31 row_mask:0xc bank_mask:0xf
	s_nop 1
	v_readlane_b32 s20, v28, 63
	s_nop 1
	s_nop 0
	v_mov_b32_e32 v17, s20
	v_max_f32_e32 v17, 0x179abe15, v17
	v_rsq_f32_e32 v28, v17
	v_exp_f32_e32 v17, v11
	v_mul_f32_e32 v25, v25, v28
	v_rcp_f32_e32 v29, v17
	v_fma_f32 v28, v173, v10, 1.0
	v_mul_f32_e32 v26, v26, v25
	v_mul_f32_e64 v25, v15, -v25
	v_pk_mul_f32 v[10:11], v[4:5], v[28:29]
	v_cvt_pk_bf16_f32 v4, v25, s0
	ds_write_b16 v130, v4 offset:52992
	v_mul_f32_e32 v4, v34, v17
	v_cvt_pk_bf16_f32 v4, v4, s0
	v_add_u32_e32 v15, 0x11700, v130
	ds_write_b16 v15, v4
	v_mul_f32_e32 v4, v29, v26
	v_cvt_pk_bf16_f32 v4, v4, s0
	v_add_u32_e32 v15, 0x13b00, v130
	ds_write_b16 v15, v4
	v_mul_f32_e32 v4, v10, v29
	v_cvt_pk_bf16_f32 v4, v4, s0
	v_add_u32_e32 v15, 0x15f00, v130
	ds_write_b16 v15, v4
	v_mul_f32_e32 v4, v34, v10
	v_mul_f32_e32 v15, v174, v4
	v_mov_b32_e32 v28, v1
	s_nop 1
	v_mov_b32_dpp v28, v15 quad_perm:[1,0,3,2] row_mask:0xf bank_mask:0xf
	v_fmac_f32_e32 v28, v174, v4
	s_nop 1
	v_add_f32_dpp v4, v28, v28 quad_perm:[2,3,0,1] row_mask:0xf bank_mask:0xf bound_ctrl:1
	s_nop 1
	v_add_f32_dpp v4, v4, v4 row_half_mirror row_mask:0xf bank_mask:0xf bound_ctrl:1
	s_nop 1
	v_add_f32_dpp v4, v4, v4 row_mirror row_mask:0xf bank_mask:0xf bound_ctrl:1
	s_nop 0
	v_readlane_b32 s20, v4, 0
	v_readlane_b32 s42, v4, 16
	v_readlane_b32 s21, v4, 32
	v_readlane_b32 s53, v4, 48
	s_and_saveexec_b64 s[14:15], s[36:37]
	s_cbranch_execz .LBB0_707
	v_readlane_b32 s56, v254, 61
	s_add_i32 s56, s29, s56
	s_ashr_i32 s57, s56, 31
	s_lshl_b64 s[56:57], s[56:57], 5
	v_mov_b32_e32 v28, s42
	v_mov_b32_e32 v29, s53
	s_add_u32 s56, s22, s56
	v_pk_add_f32 v[28:29], s[20:21], v[28:29]
	s_addc_u32 s57, s28, s57
	v_add_f32_e32 v4, v28, v29
	global_store_dword v1, v4, s[56:57]
; __device__ __forceinline__ float bf2f(unsigned v) { return __uint_as_float(v << 16); }
; #define DPPF(v, ctrl) __int_as_float(__builtin_amdgcn_update_dpp(0, __float_as_int(v), (ctrl), 0xf, 0xf, false))
; __device__ __forceinline__ void lds_st_bf16(LAS unsigned char* base, int idx, float v) { *(LAS bf16_t*)(base + idx * 2) = (bf16_t)f2bf(v); }
; __device__ __forceinline__ float row16_sum(float v) {
;     v += DPPF(v, 0xB1); v += DPPF(v, 0x4E); v += DPPF(v, 0x141); v += DPPF(v, 0x140); return v;
; }
; __device__ __forceinline__ float wave_sum(float v) {
;     v = row16_sum(v);
;     const int iv = __float_as_int(v);
;     return (__int_as_float(__builtin_amdgcn_readlane(iv, 0)) + __int_as_float(__builtin_amdgcn_readlane(iv, 16))) + (__int_as_float(__builtin_amdgcn_readlane(iv, 32)) + __int_as_float(__builtin_amdgcn_readlane(iv, 48)));
; }
; __device__ __forceinline__ void phase_rwkv_chunk(const Ctx& c, const Args& a, int layer, const bf16_t* proj, const bf16_t* wlb, const bf16_t* alb, bf16_t* rwu, float* bonusg) {
;     ...
;             for (int i = 0; i < 8; ++i) { const int tt = wave * 8 + i, t = t0 + tt;
;                 const float Lc = lcs[i] + off, al = als[i];
;                 const float rc = bf2f(rraw[i + 1]), kc = bf2f(kraw[i + 1]), vc = bf2f(vraw[i + 1]);
;                 const float r = rc + (bf2f(rraw[i]) - rc) * mur, k = kc + (bf2f(kraw[i]) - kc) * muk, v = vc + (bf2f(vraw[i]) - vc) * muv;
;                 float kk = k * kkw; const float n2 = wave_sum(kk * kk); kk = kk * rsqrtf(fmaxf(n2, 1e-24f));
;                 const float kp = k * (1.0f + (al - 1.0f) * kaw), av = -kk, bv = kk * al;
;                 const float eW = __expf(Lc), eInv = __builtin_amdgcn_rcpf(eW), eC = eTot * eInv; const float eWex = eWprev; eWprev = eW;
;                 lds_st_bf16(L + RC_AT, tt * 72 + j, av * eWex); tA[i] = av * eWex;
;                 lds_st_bf16(L + RC_RT, tt * 72 + j, r * eW); lds_st_bf16(L + RC_BT, tt * 72 + j, bv * eInv); lds_st_bf16(L + RC_KT, tt * 72 + j, kp * eInv);
;                 tV[i] = v; tB[i] = bv * eC; tK[i] = kp * eC;
;                 const float bon = wave_sum(r * kp * rk); if (lane == 0) bonusg[(size_t)t * 8 + h] = bon; }
.LBB0_707:
	s_or_b64 exec, exec, s[14:15]
	v_lshlrev_b32_e32 v4, 16, v45
	v_add_f32_e32 v4, v171, v4
	v_mul_f32_e32 v4, 0xbfb8aa3b, v4
	v_exp_f32_e32 v4, v4
	v_lshlrev_b32_e32 v34, 16, v65
	v_mov_b32_e32 v29, v1
	v_add_f32_e32 v13, v13, v22
	v_add_f32_e32 v4, 1.0, v4
	v_rcp_f32_e32 v35, v4
	v_sub_f32_e32 v4, v27, v34
	v_fma_f32 v4, v4, v176, v34
	v_mul_f32_e32 v27, v4, v172
	v_mul_f32_e32 v28, v27, v27
	v_mul_f32_e32 v13, 0x3fb8aa3b, v13
	v_lshlrev_b32_e32 v15, 16, v68
	v_mov_b32_dpp v29, v28 quad_perm:[1,0,3,2] row_mask:0xf bank_mask:0xf
	v_fmac_f32_e32 v29, v27, v27
	v_sub_f32_e32 v12, v12, v15
	v_fma_f32 v180, v12, v175, v15
	v_add_f32_dpp v28, v29, v29 quad_perm:[2,3,0,1] row_mask:0xf bank_mask:0xf bound_ctrl:1
	v_add_f32_e32 v12, -1.0, v35
	v_fma_f32 v178, v173, v12, 1.0
	v_add_f32_dpp v28, v28, v28 row_half_mirror row_mask:0xf bank_mask:0xf bound_ctrl:1
	s_nop 1
	v_add_f32_dpp v28, v28, v28 row_mirror row_mask:0xf bank_mask:0xf bound_ctrl:1
	s_nop 0
	s_nop 1
	v_add_f32_dpp v28, v28, v28 row_bcast:15 row_mask:0xa bank_mask:0xf
	s_nop 1
	v_add_f32_dpp v28, v28, v28 row_bcast:31 row_mask:0xc bank_mask:0xf
	s_nop 1
	v_readlane_b32 s20, v28, 63
	s_nop 1
	s_nop 0
	v_mov_b32_e32 v28, s20
	v_exp_f32_e32 v29, v13
	v_max_f32_e32 v28, 0x179abe15, v28
	v_rsq_f32_e32 v28, v28
	v_rcp_f32_e32 v179, v29
	v_mul_f32_e32 v27, v27, v28
	v_mul_f32_e32 v28, v35, v27
	v_mul_f32_e64 v27, v17, -v27
	v_pk_mul_f32 v[12:13], v[4:5], v[178:179]
	v_cvt_pk_bf16_f32 v4, v27, s0
	ds_write_b16 v131, v4 offset:52992
	v_mul_f32_e32 v4, v180, v29
	v_cvt_pk_bf16_f32 v4, v4, s0
	v_add_u32_e32 v17, 0x11700, v131
	ds_write_b16 v17, v4
	v_mul_f32_e32 v4, v179, v28
	v_cvt_pk_bf16_f32 v4, v4, s0
	v_add_u32_e32 v17, 0x13b00, v131
	ds_write_b16 v17, v4
	v_mul_f32_e32 v4, v12, v179
	v_cvt_pk_bf16_f32 v4, v4, s0
	v_add_u32_e32 v17, 0x15f00, v131
	ds_write_b16 v17, v4
	v_mul_f32_e32 v4, v180, v12
	v_mul_f32_e32 v17, v174, v4
	v_mov_b32_e32 v35, v1
	s_nop 1
	v_mov_b32_dpp v35, v17 quad_perm:[1,0,3,2] row_mask:0xf bank_mask:0xf
	v_fmac_f32_e32 v35, v174, v4
	s_nop 1
	v_add_f32_dpp v4, v35, v35 quad_perm:[2,3,0,1] row_mask:0xf bank_mask:0xf bound_ctrl:1
	s_nop 1
	v_add_f32_dpp v4, v4, v4 row_half_mirror row_mask:0xf bank_mask:0xf bound_ctrl:1
	s_nop 1
	v_add_f32_dpp v4, v4, v4 row_mirror row_mask:0xf bank_mask:0xf bound_ctrl:1
	s_nop 0
	v_readlane_b32 s20, v4, 0
	v_readlane_b32 s42, v4, 16
	v_readlane_b32 s21, v4, 32
	v_readlane_b32 s53, v4, 48
	s_and_saveexec_b64 s[14:15], s[36:37]
	s_cbranch_execz .LBB0_709
	v_readlane_b32 s56, v254, 62
	s_add_i32 s56, s29, s56
	s_ashr_i32 s57, s56, 31
	s_lshl_b64 s[56:57], s[56:57], 5
	v_mov_b32_e32 v178, s42
	v_mov_b32_e32 v179, s53
	s_add_u32 s56, s22, s56
	v_pk_add_f32 v[178:179], s[20:21], v[178:179]
	s_addc_u32 s57, s28, s57
	v_add_f32_e32 v4, v178, v179
	global_store_dword v1, v4, s[56:57]
.LBB0_709:
	s_or_b64 exec, exec, s[14:15]
	v_lshlrev_b32_e32 v4, 16, v51
	v_add_f32_e32 v4, v171, v4
	v_mul_f32_e32 v4, 0xbfb8aa3b, v4
	v_exp_f32_e32 v4, v4
	v_lshlrev_b32_e32 v178, 16, v72
	v_mov_b32_e32 v35, v1
	v_add_f32_e32 v14, v22, v14
	v_add_f32_e32 v4, 1.0, v4
	v_rcp_f32_e32 v179, v4
	v_sub_f32_e32 v4, v34, v178
	v_fma_f32 v4, v4, v176, v178
	v_mul_f32_e32 v180, v4, v172
	v_mul_f32_e32 v34, v180, v180
	v_mul_f32_e32 v14, 0x3fb8aa3b, v14
	v_lshlrev_b32_e32 v17, 16, v70
	v_mov_b32_dpp v35, v34 quad_perm:[1,0,3,2] row_mask:0xf bank_mask:0xf
	v_fmac_f32_e32 v35, v180, v180
	s_nop 1
	v_add_f32_dpp v34, v35, v35 quad_perm:[2,3,0,1] row_mask:0xf bank_mask:0xf bound_ctrl:1
	s_nop 1
	v_add_f32_dpp v34, v34, v34 row_half_mirror row_mask:0xf bank_mask:0xf bound_ctrl:1
	s_nop 1
	v_add_f32_dpp v34, v34, v34 row_mirror row_mask:0xf bank_mask:0xf bound_ctrl:1
	s_nop 0
	s_nop 1
	v_add_f32_dpp v34, v34, v34 row_bcast:15 row_mask:0xa bank_mask:0xf
	s_nop 1
	v_add_f32_dpp v34, v34, v34 row_bcast:31 row_mask:0xc bank_mask:0xf
	s_nop 1
	v_readlane_b32 s20, v34, 63
	s_nop 1
	s_nop 0
	v_mov_b32_e32 v34, s20
	v_exp_f32_e32 v35, v14
	v_max_f32_e32 v34, 0x179abe15, v34
	v_rsq_f32_e32 v34, v34
	v_sub_f32_e32 v14, v15, v17
	v_rcp_f32_e32 v181, v35
	v_fma_f32 v182, v14, v175, v17
	v_mul_f32_e32 v183, v180, v34
	v_add_f32_e32 v14, -1.0, v179
	v_fma_f32 v180, v173, v14, 1.0
	v_mul_f32_e64 v29, v29, -v183
	v_pk_mul_f32 v[14:15], v[4:5], v[180:181]
	v_cvt_pk_bf16_f32 v4, v29, s0
	ds_write_b16 v132, v4 offset:52992
	v_mul_f32_e32 v4, v182, v35
	v_mul_f32_e32 v34, v179, v183
	v_cvt_pk_bf16_f32 v4, v4, s0
	v_add_u32_e32 v179, 0x11700, v132
	ds_write_b16 v179, v4
	v_mul_f32_e32 v4, v181, v34
	v_cvt_pk_bf16_f32 v4, v4, s0
	v_add_u32_e32 v179, 0x13b00, v132
	ds_write_b16 v179, v4
	v_mul_f32_e32 v4, v14, v181
	v_cvt_pk_bf16_f32 v4, v4, s0
	v_add_u32_e32 v179, 0x15f00, v132
	ds_write_b16 v179, v4
	v_mul_f32_e32 v4, v182, v14
	v_mul_f32_e32 v179, v174, v4
	v_mov_b32_e32 v180, v1
	s_nop 1
	v_mov_b32_dpp v180, v179 quad_perm:[1,0,3,2] row_mask:0xf bank_mask:0xf
	v_fmac_f32_e32 v180, v174, v4
	s_nop 1
	v_add_f32_dpp v4, v180, v180 quad_perm:[2,3,0,1] row_mask:0xf bank_mask:0xf bound_ctrl:1
	s_nop 1
	v_add_f32_dpp v4, v4, v4 row_half_mirror row_mask:0xf bank_mask:0xf bound_ctrl:1
	s_nop 1
	v_add_f32_dpp v4, v4, v4 row_mirror row_mask:0xf bank_mask:0xf bound_ctrl:1
	s_nop 0
	v_readlane_b32 s20, v4, 0
	v_readlane_b32 s42, v4, 16
	v_readlane_b32 s21, v4, 32
	v_readlane_b32 s53, v4, 48
	s_and_saveexec_b64 s[14:15], s[36:37]
	s_cbranch_execz .LBB0_711
	v_readlane_b32 s56, v254, 63
	s_add_i32 s56, s29, s56
	s_ashr_i32 s57, s56, 31
	s_lshl_b64 s[56:57], s[56:57], 5
	v_mov_b32_e32 v180, s42
	v_mov_b32_e32 v181, s53
	s_add_u32 s56, s22, s56
	v_pk_add_f32 v[180:181], s[20:21], v[180:181]
	s_addc_u32 s57, s28, s57
	v_add_f32_e32 v4, v180, v181
	global_store_dword v1, v4, s[56:57]
; __device__ __forceinline__ float bf2f(unsigned v) { return __uint_as_float(v << 16); }
; #define DPPF(v, ctrl) __int_as_float(__builtin_amdgcn_update_dpp(0, __float_as_int(v), (ctrl), 0xf, 0xf, false))
; __device__ __forceinline__ void lds_st_bf16(LAS unsigned char* base, int idx, float v) { *(LAS bf16_t*)(base + idx * 2) = (bf16_t)f2bf(v); }
; __device__ __forceinline__ float row16_sum(float v) {
;     v += DPPF(v, 0xB1); v += DPPF(v, 0x4E); v += DPPF(v, 0x141); v += DPPF(v, 0x140); return v;
; }
; __device__ __forceinline__ float wave_sum(float v) {
;     v = row16_sum(v);
;     const int iv = __float_as_int(v);
;     return (__int_as_float(__builtin_amdgcn_readlane(iv, 0)) + __int_as_float(__builtin_amdgcn_readlane(iv, 16))) + (__int_as_float(__builtin_amdgcn_readlane(iv, 32)) + __int_as_float(__builtin_amdgcn_readlane(iv, 48)));
; }
; __device__ __forceinline__ void phase_rwkv_chunk(const Ctx& c, const Args& a, int layer, const bf16_t* proj, const bf16_t* wlb, const bf16_t* alb, bf16_t* rwu, float* bonusg) {
;     ...
;             for (int i = 0; i < 8; ++i) { const int tt = wave * 8 + i, t = t0 + tt;
;                 const float Lc = lcs[i] + off, al = als[i];
;                 const float rc = bf2f(rraw[i + 1]), kc = bf2f(kraw[i + 1]), vc = bf2f(vraw[i + 1]);
;                 const float r = rc + (bf2f(rraw[i]) - rc) * mur, k = kc + (bf2f(kraw[i]) - kc) * muk, v = vc + (bf2f(vraw[i]) - vc) * muv;
;                 float kk = k * kkw; const float n2 = wave_sum(kk * kk); kk = kk * rsqrtf(fmaxf(n2, 1e-24f));
;                 const float kp = k * (1.0f + (al - 1.0f) * kaw), av = -kk, bv = kk * al;
;                 const float eW = __expf(Lc), eInv = __builtin_amdgcn_rcpf(eW), eC = eTot * eInv; const float eWex = eWprev; eWprev = eW;
;                 lds_st_bf16(L + RC_AT, tt * 72 + j, av * eWex); tA[i] = av * eWex;
;                 lds_st_bf16(L + RC_RT, tt * 72 + j, r * eW); lds_st_bf16(L + RC_BT, tt * 72 + j, bv * eInv); lds_st_bf16(L + RC_KT, tt * 72 + j, kp * eInv);
;                 tV[i] = v; tB[i] = bv * eC; tK[i] = kp * eC;
;                 const float bon = wave_sum(r * kp * rk); if (lane == 0) bonusg[(size_t)t * 8 + h] = bon; }
.LBB0_711:
	s_or_b64 exec, exec, s[14:15]
	v_lshlrev_b32_e32 v4, 16, v54
	v_add_f32_e32 v4, v171, v4
	v_mul_f32_e32 v4, 0xbfb8aa3b, v4
	v_exp_f32_e32 v4, v4
	v_lshlrev_b32_e32 v180, 16, v71
	v_mov_b32_e32 v179, v1
	v_add_f32_e32 v16, v22, v16
	v_add_f32_e32 v4, 1.0, v4
	v_rcp_f32_e32 v184, v4
	v_sub_f32_e32 v4, v178, v180
	v_fma_f32 v4, v4, v176, v180
	v_mul_f32_e32 v182, v4, v172
	v_mul_f32_e32 v178, v182, v182
	v_mul_f32_e32 v16, 0x3fb8aa3b, v16
	v_lshlrev_b32_e32 v181, 16, v77
	v_mov_b32_dpp v179, v178 quad_perm:[1,0,3,2] row_mask:0xf bank_mask:0xf
	v_fmac_f32_e32 v179, v182, v182
	s_nop 1
	v_add_f32_dpp v178, v179, v179 quad_perm:[2,3,0,1] row_mask:0xf bank_mask:0xf bound_ctrl:1
	s_nop 1
	v_add_f32_dpp v178, v178, v178 row_half_mirror row_mask:0xf bank_mask:0xf bound_ctrl:1
	s_nop 1
	v_add_f32_dpp v178, v178, v178 row_mirror row_mask:0xf bank_mask:0xf bound_ctrl:1
	s_nop 0
	s_nop 1
	v_add_f32_dpp v178, v178, v178 row_bcast:15 row_mask:0xa bank_mask:0xf
	s_nop 1
	v_add_f32_dpp v178, v178, v178 row_bcast:31 row_mask:0xc bank_mask:0xf
	s_nop 1
	v_readlane_b32 s20, v178, 63
	s_nop 1
	s_nop 0
	v_mov_b32_e32 v178, s20
	v_exp_f32_e32 v179, v16
	v_max_f32_e32 v178, 0x179abe15, v178
	v_rsq_f32_e32 v178, v178
	v_sub_f32_e32 v16, v17, v181
	v_rcp_f32_e32 v183, v179
	v_fma_f32 v185, v16, v175, v181
	v_mul_f32_e32 v187, v182, v178
	v_add_f32_e32 v16, -1.0, v184
	v_fma_f32 v182, v173, v16, 1.0
	v_mul_f32_e64 v35, v35, -v187
	v_pk_mul_f32 v[16:17], v[4:5], v[182:183]
	v_cvt_pk_bf16_f32 v4, v35, s0
	ds_write_b16 v133, v4 offset:52992
	v_mul_f32_e32 v4, v185, v179
	v_mul_f32_e32 v178, v184, v187
	v_cvt_pk_bf16_f32 v4, v4, s0
	v_add_u32_e32 v182, 0x11700, v133
	ds_write_b16 v182, v4
	v_mul_f32_e32 v4, v183, v178
	v_cvt_pk_bf16_f32 v4, v4, s0
	v_add_u32_e32 v182, 0x13b00, v133
	ds_write_b16 v182, v4
	v_mul_f32_e32 v4, v16, v183
	v_cvt_pk_bf16_f32 v4, v4, s0
	v_add_u32_e32 v182, 0x15f00, v133
	ds_write_b16 v182, v4
	v_mul_f32_e32 v4, v185, v16
	v_mul_f32_e32 v182, v174, v4
	v_mov_b32_e32 v183, v1
	s_nop 1
	v_mov_b32_dpp v183, v182 quad_perm:[1,0,3,2] row_mask:0xf bank_mask:0xf
	v_fmac_f32_e32 v183, v174, v4
	s_nop 1
	v_add_f32_dpp v4, v183, v183 quad_perm:[2,3,0,1] row_mask:0xf bank_mask:0xf bound_ctrl:1
	s_nop 1
	v_add_f32_dpp v4, v4, v4 row_half_mirror row_mask:0xf bank_mask:0xf bound_ctrl:1
	s_nop 1
	v_add_f32_dpp v4, v4, v4 row_mirror row_mask:0xf bank_mask:0xf bound_ctrl:1
	s_nop 0
	v_readlane_b32 s20, v4, 0
	v_readlane_b32 s42, v4, 16
	v_readlane_b32 s21, v4, 32
	v_readlane_b32 s53, v4, 48
	s_and_saveexec_b64 s[14:15], s[36:37]
	s_cbranch_execz .LBB0_713
	v_readlane_b32 s56, v255, 0
	s_add_i32 s56, s29, s56
	s_ashr_i32 s57, s56, 31
	s_lshl_b64 s[56:57], s[56:57], 5
	v_mov_b32_e32 v182, s42
	v_mov_b32_e32 v183, s53
	s_add_u32 s56, s22, s56
	v_pk_add_f32 v[182:183], s[20:21], v[182:183]
	s_addc_u32 s57, s28, s57
	v_add_f32_e32 v4, v182, v183
	global_store_dword v1, v4, s[56:57]
.LBB0_713:
	s_or_b64 exec, exec, s[14:15]
	v_lshlrev_b32_e32 v4, 16, v61
	v_add_f32_e32 v4, v171, v4
	v_mul_f32_e32 v4, 0xbfb8aa3b, v4
	v_exp_f32_e32 v4, v4
	v_lshlrev_b32_e32 v183, 16, v80
	v_add_f32_e32 v19, v22, v19
	v_sub_f32_e32 v22, v181, v183
	v_add_f32_e32 v4, 1.0, v4
	v_rcp_f32_e32 v182, v4
	v_lshlrev_b32_e32 v4, 16, v81
	v_fmac_f32_e32 v183, v22, v175
	v_sub_f32_e32 v22, v180, v4
	v_fmac_f32_e32 v4, v22, v176
	v_mul_f32_e32 v22, v4, v172
	v_mul_f32_e32 v180, v22, v22
	v_mov_b32_e32 v181, v1
	v_mul_f32_e32 v19, 0x3fb8aa3b, v19
	s_nop 0
	v_mov_b32_dpp v181, v180 quad_perm:[1,0,3,2] row_mask:0xf bank_mask:0xf
	v_fmac_f32_e32 v181, v22, v22
	s_nop 1
	v_add_f32_dpp v180, v181, v181 quad_perm:[2,3,0,1] row_mask:0xf bank_mask:0xf bound_ctrl:1
	s_nop 1
	v_add_f32_dpp v180, v180, v180 row_half_mirror row_mask:0xf bank_mask:0xf bound_ctrl:1
	s_nop 1
	v_add_f32_dpp v180, v180, v180 row_mirror row_mask:0xf bank_mask:0xf bound_ctrl:1
	s_nop 0
	s_nop 1
	v_add_f32_dpp v180, v180, v180 row_bcast:15 row_mask:0xa bank_mask:0xf
	s_nop 1
	v_add_f32_dpp v180, v180, v180 row_bcast:31 row_mask:0xc bank_mask:0xf
	s_nop 1
	v_readlane_b32 s20, v180, 63
	s_nop 1
	s_nop 0
	v_mov_b32_e32 v180, s20
	v_max_f32_e32 v180, 0x179abe15, v180
	v_rsq_f32_e32 v180, v180
	s_nop 0
	v_mul_f32_e32 v184, v22, v180
	v_add_f32_e32 v22, -1.0, v182
	v_fma_f32 v180, v173, v22, 1.0
	v_mul_f32_e32 v22, v182, v184
	v_exp_f32_e32 v182, v19
	v_mul_f32_e64 v19, v179, -v184
	v_cvt_pk_bf16_f32 v179, v19, s0
	ds_write_b16 v134, v179 offset:52992
	v_rcp_f32_e32 v181, v182
	v_mul_f32_e32 v179, v183, v182
	v_cvt_pk_bf16_f32 v179, v179, s0
	v_pk_mul_f32 v[4:5], v[4:5], v[180:181]
	v_add_u32_e32 v180, 0x11700, v134
	ds_write_b16 v180, v179
	v_mul_f32_e32 v179, v181, v22
	v_cvt_pk_bf16_f32 v179, v179, s0
	v_add_u32_e32 v180, 0x13b00, v134
	ds_write_b16 v180, v179
	v_mul_f32_e32 v179, v4, v181
	v_cvt_pk_bf16_f32 v179, v179, s0
	v_add_u32_e32 v180, 0x15f00, v134
	ds_write_b16 v180, v179
	v_mul_f32_e32 v179, v183, v4
	v_mul_f32_e32 v180, v174, v179
	v_mov_b32_e32 v181, v1
	s_nop 1
	v_mov_b32_dpp v181, v180 quad_perm:[1,0,3,2] row_mask:0xf bank_mask:0xf
	v_fmac_f32_e32 v181, v174, v179
	s_nop 1
	v_add_f32_dpp v179, v181, v181 quad_perm:[2,3,0,1] row_mask:0xf bank_mask:0xf bound_ctrl:1
	s_nop 1
	v_add_f32_dpp v179, v179, v179 row_half_mirror row_mask:0xf bank_mask:0xf bound_ctrl:1
	s_nop 1
	v_add_f32_dpp v179, v179, v179 row_mirror row_mask:0xf bank_mask:0xf bound_ctrl:1
	s_nop 0
	v_readlane_b32 s20, v179, 0
	v_readlane_b32 s42, v179, 16
	v_readlane_b32 s21, v179, 32
	v_readlane_b32 s53, v179, 48
	s_and_saveexec_b64 s[14:15], s[36:37]
	s_cbranch_execz .LBB0_715
	v_readlane_b32 s56, v255, 1
	s_add_i32 s56, s29, s56
	s_ashr_i32 s57, s56, 31
	s_lshl_b64 s[56:57], s[56:57], 5
	v_mov_b32_e32 v180, s42
	v_mov_b32_e32 v181, s53
	s_add_u32 s56, s22, s56
	v_pk_add_f32 v[180:181], s[20:21], v[180:181]
	s_addc_u32 s57, s28, s57
	v_add_f32_e32 v179, v180, v181
	global_store_dword v1, v179, s[56:57]
